# merge phase: all 32 operand loads of the fnet output projection issued up front (one wait) instead of hipcc's dribbled rotation through a few registers
# speedup vs baseline: 1.0015x; 1.0015x over previous
; __device__ __forceinline__ void ph_merge(const Params& p, int l, LAS unsigned char* lds) {
;     ...
;         f32x16 O0, O1;
;         {
; #pragma unroll
;             for (int q = 0; q < 16; ++q) { O0[q] = 0.f; O1[q] = 0.f; }
;             const size_t row = ((((size_t)b * 128 + wv * 16 + 2 * h2) * 2) * 2048 + s0 + r) * 4;
;             u32x4 u0[8];
; #pragma unroll
;             for (int s = 0; s < 8; ++s) { const size_t o = row + (size_t)(s & 3) * (4 * 2 * 2048 * 4) + (size_t)(s >> 2) * (2048 * 4);
;                 const u32x2 lo = *(const u32x2*)(UV + o), hi = *(const u32x2*)(UV + o + 2 * 2048 * 4); u0[s].x = lo.x; u0[s].y = lo.y; u0[s].z = hi.x; u0[s].w = hi.y; }
;             bf16x8 af0[8], af1[8];
; #pragma unroll
;             for (int s = 0; s < 8; ++s) { af0[s] = *(const bf16x8*)(ABT + (size_t)r * 128 + 16 * s + 8 * h2); af1[s] = *(const bf16x8*)(ABT + (size_t)(32 + r) * 128 + 16 * s + 8 * h2); }
; #pragma unroll
;             for (int s = 0; s < 8; ++s) {
;                 const bf16x8 bfr = __builtin_bit_cast(bf16x8, u0[s]);
;                 O0 = __builtin_amdgcn_mfma_f32_32x32x16_bf16(af0[s], bfr, O0, 0, 0, 0);
;                 O1 = __builtin_amdgcn_mfma_f32_32x32x16_bf16(af1[s], bfr, O1, 0, 0, 0);
;             }
;             float ss = 0.f;
; #pragma unroll
;             for (int q = 0; q < 16; ++q) ss += O0[q] * O0[q] + O1[q] * O1[q];
;             ss += __shfl_xor(ss, 32);
;             if (h2 == 0) ssA[wv * 32 + r] = ss;
.LBB0_1040:
	s_ashr_i32 s10, s8, 6
	s_ashr_i32 s11, s10, 31
	s_lshl_b64 s[10:11], s[10:11], 19
	s_and_b32 s9, s4, 0x7e0
	v_lshl_add_u64 v[2:3], s[10:11], 0, v[124:125]
	v_or_b32_e32 v2, s9, v2
	v_readlane_b32 s10, v253, 41
	v_or_b32_e32 v2, v2, v106
	v_readlane_b32 s11, v253, 42
	v_lshlrev_b32_e32 v98, 3, v2
	global_load_dwordx4 v[34:37], v[108:109], off
	global_load_dwordx4 v[66:69], v[110:111], off
	global_load_dwordx4 v[38:41], v[108:109], off offset:32
	global_load_dwordx4 v[70:73], v[110:111], off offset:32
	global_load_dwordx4 v[42:45], v[108:109], off offset:64
	global_load_dwordx4 v[74:77], v[110:111], off offset:64
	global_load_dwordx4 v[46:49], v[108:109], off offset:96
	global_load_dwordx4 v[78:81], v[110:111], off offset:96
	global_load_dwordx4 v[50:53], v[108:109], off offset:128
	global_load_dwordx4 v[82:85], v[110:111], off offset:128
	global_load_dwordx4 v[54:57], v[108:109], off offset:160
	global_load_dwordx4 v[86:89], v[110:111], off offset:160
	global_load_dwordx4 v[58:61], v[108:109], off offset:192
	global_load_dwordx4 v[90:93], v[110:111], off offset:192
	global_load_dwordx4 v[62:65], v[108:109], off offset:224
	global_load_dwordx4 v[94:97], v[110:111], off offset:224
	v_mov_b32_e32 v142, v98
	v_add_u32_e32 v144, 0x8000, v98
	global_load_dwordx2 v[142:143], v142, s[10:11]
	global_load_dwordx2 v[144:145], v144, s[10:11]
	v_add_u32_e32 v146, 0x20000, v98
	v_add_u32_e32 v148, 0x28000, v98
	global_load_dwordx2 v[146:147], v146, s[10:11]
	global_load_dwordx2 v[148:149], v148, s[10:11]
	v_add_u32_e32 v150, 0x40000, v98
	v_add_u32_e32 v152, 0x48000, v98
	global_load_dwordx2 v[150:151], v150, s[10:11]
	global_load_dwordx2 v[152:153], v152, s[10:11]
	v_add_u32_e32 v154, 0x60000, v98
	v_add_u32_e32 v156, 0x68000, v98
	global_load_dwordx2 v[154:155], v154, s[10:11]
	global_load_dwordx2 v[156:157], v156, s[10:11]
	v_add_u32_e32 v158, 0x4000, v98
	v_add_u32_e32 v160, 0xc000, v98
	global_load_dwordx2 v[158:159], v158, s[10:11]
	global_load_dwordx2 v[160:161], v160, s[10:11]
	v_add_u32_e32 v162, 0x24000, v98
	v_add_u32_e32 v164, 0x2c000, v98
	global_load_dwordx2 v[162:163], v162, s[10:11]
	global_load_dwordx2 v[164:165], v164, s[10:11]
	v_add_u32_e32 v166, 0x44000, v98
	v_add_u32_e32 v168, 0x4c000, v98
	global_load_dwordx2 v[166:167], v166, s[10:11]
	global_load_dwordx2 v[168:169], v168, s[10:11]
	v_add_u32_e32 v170, 0x64000, v98
	v_add_u32_e32 v172, 0x6c000, v98
	global_load_dwordx2 v[170:171], v170, s[10:11]
	global_load_dwordx2 v[172:173], v172, s[10:11]
	s_waitcnt vmcnt(0)
	v_mfma_f32_32x32x16_bf16 v[18:33], v[34:37], v[142:145], 0
	v_mfma_f32_32x32x16_bf16 v[2:17], v[66:69], v[142:145], 0
	v_mfma_f32_32x32x16_bf16 v[18:33], v[38:41], v[146:149], v[18:33]
	v_mfma_f32_32x32x16_bf16 v[2:17], v[70:73], v[146:149], v[2:17]
	v_mfma_f32_32x32x16_bf16 v[18:33], v[42:45], v[150:153], v[18:33]
	v_mfma_f32_32x32x16_bf16 v[2:17], v[74:77], v[150:153], v[2:17]
	v_mfma_f32_32x32x16_bf16 v[18:33], v[46:49], v[154:157], v[18:33]
	v_mfma_f32_32x32x16_bf16 v[2:17], v[78:81], v[154:157], v[2:17]
	v_mfma_f32_32x32x16_bf16 v[18:33], v[50:53], v[158:161], v[18:33]
	v_mfma_f32_32x32x16_bf16 v[2:17], v[82:85], v[158:161], v[2:17]
	v_mfma_f32_32x32x16_bf16 v[18:33], v[54:57], v[162:165], v[18:33]
	v_mfma_f32_32x32x16_bf16 v[2:17], v[86:89], v[162:165], v[2:17]
	v_mfma_f32_32x32x16_bf16 v[2:17], v[90:93], v[166:169], v[2:17]
	v_mfma_f32_32x32x16_bf16 v[18:33], v[58:61], v[166:169], v[18:33]
	v_mfma_f32_32x32x16_bf16 v[2:17], v[94:97], v[170:173], v[2:17]
	s_nop 11
	v_mul_f32_e32 v38, v6, v6
	v_mfma_f32_32x32x16_bf16 v[18:33], v[62:65], v[170:173], v[18:33]
	v_mul_f32_e32 v34, v2, v2
	v_mul_f32_e32 v35, v3, v3
	v_mul_f32_e32 v36, v4, v4
	v_mul_f32_e32 v37, v5, v5
	v_mul_f32_e32 v39, v7, v7
	v_mul_f32_e32 v40, v8, v8
	v_mul_f32_e32 v41, v9, v9
	s_nop 4
	v_fmac_f32_e32 v34, v18, v18
	v_fmac_f32_e32 v35, v19, v19
	v_fmac_f32_e32 v36, v20, v20
	v_add_f32_e32 v34, v34, v35
	v_fmac_f32_e32 v37, v21, v21
	v_add_f32_e32 v34, v36, v34
	v_fmac_f32_e32 v38, v22, v22
	v_add_f32_e32 v34, v37, v34
	v_fmac_f32_e32 v39, v23, v23
	v_add_f32_e32 v34, v38, v34
	v_fmac_f32_e32 v40, v24, v24
	v_add_f32_e32 v34, v39, v34
	v_mul_f32_e32 v42, v10, v10
	v_fmac_f32_e32 v41, v25, v25
	v_add_f32_e32 v34, v40, v34
	v_mul_f32_e32 v43, v11, v11
	v_fmac_f32_e32 v42, v26, v26
	v_add_f32_e32 v34, v41, v34
	v_mul_f32_e32 v44, v12, v12
	v_fmac_f32_e32 v43, v27, v27
	v_add_f32_e32 v34, v42, v34
	v_mul_f32_e32 v45, v13, v13
	v_fmac_f32_e32 v44, v28, v28
	v_add_f32_e32 v34, v43, v34
	v_mul_f32_e32 v46, v14, v14
	v_fmac_f32_e32 v45, v29, v29
	v_add_f32_e32 v34, v44, v34
	v_fmac_f32_e32 v46, v30, v30
	v_add_f32_e32 v34, v45, v34
	v_mul_f32_e32 v35, v15, v15
	v_add_f32_e32 v34, v46, v34
	v_fmac_f32_e32 v35, v31, v31
	v_add_f32_e32 v34, v35, v34
	v_mul_f32_e32 v35, v16, v16
	v_fmac_f32_e32 v35, v32, v32
	v_add_f32_e32 v34, v35, v34
	v_mul_f32_e32 v35, v17, v17
	v_fmac_f32_e32 v35, v33, v33
	v_add_f32_e32 v34, v35, v34
	ds_bpermute_b32 v35, v107, v34
	s_and_saveexec_b64 s[12:13], s[34:35]
	s_cbranch_execz .LBB0_1039
	s_waitcnt lgkmcnt(0)
	v_add_f32_e32 v34, v34, v35
	ds_write_b32 v140, v34
	s_branch .LBB0_1039
